# v15 + grid barrier: the globally-last arriver releases every XCD generation word itself, other XCD-last arrivers wait on their own word (one relay hop less)
# speedup vs baseline: 1.0089x; 1.0052x over previous
; __device__ __forceinline__ unsigned xb_ld(unsigned* p)              { return __hip_atomic_load(p, __ATOMIC_RELAXED, __HIP_MEMORY_SCOPE_AGENT); }
; __device__ __forceinline__ unsigned xb_add(unsigned* p, unsigned v) { return __hip_atomic_fetch_add(p, v, __ATOMIC_RELAXED, __HIP_MEMORY_SCOPE_AGENT); }
; #define XB_SPIN(cond, bar) do { unsigned _sp = 0; while (cond) { __builtin_amdgcn_s_sleep(1); \
;     if ((++_sp & 255u) == 0u) { if (xb_ld(&(bar)[XB_TMO])) break; if (_sp > XB_SPIN_CAP) { atomicAdd(&(bar)[XB_TMO], 1u); break; } } } } while (0)
; __device__ __forceinline__ void xcd_barrier(const XcdBarrier& b) {
;     ...
;         const unsigned old = xb_add(&bar[XB_XSUB(b.x)], 1u);
;         const unsigned gen = old / nloc;
;         if (old + 1u == (gen + 1u) * nloc) {
;             __builtin_amdgcn_fence(__ATOMIC_RELEASE, "agent");
;             asm volatile("s_waitcnt vmcnt(0)" ::: "memory");
;             const unsigned og = xb_add(&bar[XB_TOP], 1u);
;             const unsigned tg = og / nx;
;             if (og + 1u == (tg + 1u) * nx) xb_add(&bar[XB_TOPGEN], 1u);
;             else XB_SPIN(xb_ld(&bar[XB_TOPGEN]) == tg, bar);
;             __builtin_amdgcn_fence(__ATOMIC_ACQUIRE, "agent");
;             xb_add(&bar[XB_XGEN(b.x)], 1u);
;             asm volatile("s_waitcnt vmcnt(0)" ::: "memory");
;         } else {
;             XB_SPIN(xb_ld(&bar[XB_XGEN(b.x)]) == gen, bar);
.LBB0_152:
	s_or_b64 exec, exec, s[12:13]
	v_cvt_f32_u32_e32 v5, v3
	s_waitcnt vmcnt(0)
	v_readfirstlane_b32 s9, v4
	v_sub_u32_e32 v4, 0, v3
	v_rcp_iflag_f32_e32 v5, v5
	v_add_u32_e32 v6, s9, v2
	v_mul_f32_e32 v5, 0x4f7ffffe, v5
	v_cvt_u32_f32_e32 v5, v5
	v_mul_lo_u32 v2, v4, v5
	v_mul_hi_u32 v2, v5, v2
	v_add_u32_e32 v2, v5, v2
	v_mul_hi_u32 v2, v6, v2
	v_mul_lo_u32 v4, v2, v3
	v_sub_u32_e32 v4, v6, v4
	v_add_u32_e32 v5, 1, v2
	v_cmp_ge_u32_e32 vcc, v4, v3
	s_nop 1
	v_cndmask_b32_e32 v2, v2, v5, vcc
	v_sub_u32_e32 v5, v4, v3
	v_cndmask_b32_e32 v4, v4, v5, vcc
	v_add_u32_e32 v5, 1, v2
	v_cmp_ge_u32_e32 vcc, v4, v3
	v_add_u32_e32 v4, 1, v6
	s_nop 0
	v_cndmask_b32_e32 v2, v2, v5, vcc
	v_mul_lo_u32 v5, v3, v2
	v_add_u32_e32 v3, v5, v3
	v_cmp_ne_u32_e32 vcc, v4, v3
	v_mov_b32_e32 v19, v2
	s_and_saveexec_b64 s[10:11], vcc
	s_xor_b64 s[10:11], exec, s[10:11]
	s_cbranch_execz .LBB0_166
	s_waitcnt lgkmcnt(0)
	v_mov_b32_e32 v1, 0x2000
	global_load_dword v1, v1, s[4:5] offset:1024 sc1
	s_add_u32 s16, s4, 0x2400
	s_addc_u32 s17, s5, 0
	s_waitcnt vmcnt(0)
	v_cmp_eq_u32_e32 vcc, v1, v2
	s_and_saveexec_b64 s[12:13], vcc
	s_cbranch_execz .LBB0_165
	s_add_u32 s14, s26, 0x4200
	s_addc_u32 s15, s27, 0
	s_mov_b32 s9, 1
	s_mov_b64 s[18:19], 0
	v_mov_b32_e32 v1, 0
	s_branch .LBB0_156

; __device__ __forceinline__ unsigned xb_ld(unsigned* p)              { return __hip_atomic_load(p, __ATOMIC_RELAXED, __HIP_MEMORY_SCOPE_AGENT); }
; __device__ __forceinline__ unsigned xb_add(unsigned* p, unsigned v) { return __hip_atomic_fetch_add(p, v, __ATOMIC_RELAXED, __HIP_MEMORY_SCOPE_AGENT); }
; #define XB_SPIN(cond, bar) do { unsigned _sp = 0; while (cond) { __builtin_amdgcn_s_sleep(1); \
;     if ((++_sp & 255u) == 0u) { if (xb_ld(&(bar)[XB_TMO])) break; if (_sp > XB_SPIN_CAP) { atomicAdd(&(bar)[XB_TMO], 1u); break; } } } } while (0)
; __device__ __forceinline__ void xcd_barrier(const XcdBarrier& b) {
;     ...
;             const unsigned og = xb_add(&bar[XB_TOP], 1u);
;             const unsigned tg = og / nx;
;             if (og + 1u == (tg + 1u) * nx) xb_add(&bar[XB_TOPGEN], 1u);
;             else XB_SPIN(xb_ld(&bar[XB_TOPGEN]) == tg, bar);
.LBB0_169:
	s_or_b64 exec, exec, s[12:13]
	v_cvt_f32_u32_e32 v4, v1
	s_waitcnt vmcnt(0)
	v_readfirstlane_b32 s9, v3
	s_add_u32 s12, s26, 0x7500
	s_addc_u32 s13, s27, 0
	v_rcp_iflag_f32_e32 v4, v4
	v_add_u32_e32 v2, s9, v2
	v_add_u32_e32 v5, 1, v2
	s_mov_b64 s[14:15], -1
	v_mul_f32_e32 v3, 0x4f7ffffe, v4
	v_cvt_u32_f32_e32 v3, v3
	v_sub_u32_e32 v4, 0, v1
	v_mul_lo_u32 v4, v4, v3
	v_mul_hi_u32 v4, v3, v4
	v_add_u32_e32 v3, v3, v4
	v_mul_hi_u32 v3, v2, v3
	v_mul_lo_u32 v4, v3, v1
	v_sub_u32_e32 v2, v2, v4
	v_add_u32_e32 v6, 1, v3
	v_cmp_ge_u32_e32 vcc, v2, v1
	v_sub_u32_e32 v4, v2, v1
	s_nop 0
	v_cndmask_b32_e32 v3, v3, v6, vcc
	v_cndmask_b32_e32 v2, v2, v4, vcc
	v_add_u32_e32 v4, 1, v3
	v_cmp_ge_u32_e32 vcc, v2, v1
	s_nop 1
	v_cndmask_b32_e32 v4, v3, v4, vcc
	v_mul_lo_u32 v2, v1, v4
	v_add_u32_e32 v1, v2, v1
	v_cmp_ne_u32_e32 vcc, v5, v1
	v_mov_b64_e32 v[2:3], s[12:13]
	s_and_saveexec_b64 s[10:11], vcc
	s_cbranch_execz .LBB0_181
	v_mov_b32_e32 v1, 0
	v_mov_b32_e32 v20, 0x2000
	global_load_dword v2, v20, s[4:5] offset:1024 sc1
	s_mov_b64 s[18:19], 0
	s_waitcnt vmcnt(0)
	v_cmp_eq_u32_e32 vcc, v2, v19
	s_and_saveexec_b64 s[16:17], vcc
	s_cbranch_execz .LBB0_180
	s_add_u32 s14, s26, 0x4200
	s_addc_u32 s15, s27, 0
	s_mov_b32 s9, 1
	s_branch .LBB0_173

; __device__ __forceinline__ unsigned xb_ld(unsigned* p)              { return __hip_atomic_load(p, __ATOMIC_RELAXED, __HIP_MEMORY_SCOPE_AGENT); }
; __device__ __forceinline__ unsigned xb_add(unsigned* p, unsigned v) { return __hip_atomic_fetch_add(p, v, __ATOMIC_RELAXED, __HIP_MEMORY_SCOPE_AGENT); }
; #define XB_SPIN(cond, bar) do { unsigned _sp = 0; while (cond) { __builtin_amdgcn_s_sleep(1); \
;     if ((++_sp & 255u) == 0u) { if (xb_ld(&(bar)[XB_TMO])) break; if (_sp > XB_SPIN_CAP) { atomicAdd(&(bar)[XB_TMO], 1u); break; } } } } while (0)
; __device__ __forceinline__ void xcd_barrier(const XcdBarrier& b) {
;     ...
;             if (og + 1u == (tg + 1u) * nx) xb_add(&bar[XB_TOPGEN], 1u);
;             else XB_SPIN(xb_ld(&bar[XB_TOPGEN]) == tg, bar);
.LBB0_175:
	global_load_dword v2, v20, s[4:5] offset:1024 sc1
	s_add_i32 s9, s9, 1
	s_mov_b64 s[22:23], -1
	s_waitcnt vmcnt(0)
	v_cmp_ne_u32_e32 vcc, v2, v19
	s_orn2_b64 s[42:43], vcc, exec
	s_branch .LBB0_172

; __device__ __forceinline__ unsigned xb_ld(unsigned* p)              { return __hip_atomic_load(p, __ATOMIC_RELAXED, __HIP_MEMORY_SCOPE_AGENT); }
; __device__ __forceinline__ unsigned xb_add(unsigned* p, unsigned v) { return __hip_atomic_fetch_add(p, v, __ATOMIC_RELAXED, __HIP_MEMORY_SCOPE_AGENT); }
; #define XB_SPIN(cond, bar) do { unsigned _sp = 0; while (cond) { __builtin_amdgcn_s_sleep(1); \
;     if ((++_sp & 255u) == 0u) { if (xb_ld(&(bar)[XB_TMO])) break; if (_sp > XB_SPIN_CAP) { atomicAdd(&(bar)[XB_TMO], 1u); break; } } } } while (0)
; __device__ __forceinline__ void xcd_barrier(const XcdBarrier& b) {
;     ...
;             if (og + 1u == (tg + 1u) * nx) xb_add(&bar[XB_TOPGEN], 1u);
;             else XB_SPIN(xb_ld(&bar[XB_TOPGEN]) == tg, bar);
;             __builtin_amdgcn_fence(__ATOMIC_ACQUIRE, "agent");
;             xb_add(&bar[XB_XGEN(b.x)], 1u);
;             asm volatile("s_waitcnt vmcnt(0)" ::: "memory");
.LBB0_181:
	s_or_b64 exec, exec, s[10:11]
	s_and_saveexec_b64 s[10:11], s[14:15]
	s_cbranch_execz .LBB0_183
	v_mov_b32_e32 v1, 1
	global_atomic_add v[2:3], v1, off
	v_mov_b32_e32 v21, 0x2000
	v_mov_b32_e32 v22, 1
	s_mov_b64 s[12:13], s[28:29]
	s_movk_i32 vcc_lo, 16
.Lbh0_loop:
	global_atomic_add v21, v22, s[12:13] offset:1024
	s_add_u32 s12, s12, 0x100
	s_addc_u32 s13, s13, 0
	s_sub_i32 vcc_lo, vcc_lo, 1
	s_cmp_lg_u32 vcc_lo, 0
	s_cbranch_scc1 .Lbh0_loop
.LBB0_183:
	s_or_b64 exec, exec, s[10:11]
	s_mov_b64 s[10:11], exec
	v_mbcnt_lo_u32_b32 v1, s10, 0
	v_mbcnt_hi_u32_b32 v1, s11, v1
	v_cmp_eq_u32_e32 vcc, 0, v1
	s_waitcnt vmcnt(0)
	buffer_inv sc1
	s_and_saveexec_b64 s[12:13], vcc
	s_cbranch_execz .LBB0_185
	s_bcnt1_i32_b64 s9, s[10:11]
	v_mov_b32_e32 v1, 0x2000
	v_mov_b32_e32 v2, s9
	s_nop 0

; __device__ __forceinline__ unsigned xb_ld(unsigned* p)              { return __hip_atomic_load(p, __ATOMIC_RELAXED, __HIP_MEMORY_SCOPE_AGENT); }
; __device__ __forceinline__ unsigned xb_add(unsigned* p, unsigned v) { return __hip_atomic_fetch_add(p, v, __ATOMIC_RELAXED, __HIP_MEMORY_SCOPE_AGENT); }
; #define XB_SPIN(cond, bar) do { unsigned _sp = 0; while (cond) { __builtin_amdgcn_s_sleep(1); \
;     if ((++_sp & 255u) == 0u) { if (xb_ld(&(bar)[XB_TMO])) break; if (_sp > XB_SPIN_CAP) { atomicAdd(&(bar)[XB_TMO], 1u); break; } } } } while (0)
; __device__ __forceinline__ void xcd_barrier(const XcdBarrier& b) {
;     ...
;         const unsigned old = xb_add(&bar[XB_XSUB(b.x)], 1u);
;         const unsigned gen = old / nloc;
;         if (old + 1u == (gen + 1u) * nloc) {
;             __builtin_amdgcn_fence(__ATOMIC_RELEASE, "agent");
;             asm volatile("s_waitcnt vmcnt(0)" ::: "memory");
;             const unsigned og = xb_add(&bar[XB_TOP], 1u);
;             const unsigned tg = og / nx;
;             if (og + 1u == (tg + 1u) * nx) xb_add(&bar[XB_TOPGEN], 1u);
;             else XB_SPIN(xb_ld(&bar[XB_TOPGEN]) == tg, bar);
;             __builtin_amdgcn_fence(__ATOMIC_ACQUIRE, "agent");
;             xb_add(&bar[XB_XGEN(b.x)], 1u);
;             asm volatile("s_waitcnt vmcnt(0)" ::: "memory");
;         } else {
;             XB_SPIN(xb_ld(&bar[XB_XGEN(b.x)]) == gen, bar);
.LBB0_547:
	s_or_b64 exec, exec, s[12:13]
	v_cvt_f32_u32_e32 v5, v3
	s_waitcnt vmcnt(0)
	v_readfirstlane_b32 s9, v4
	v_sub_u32_e32 v4, 0, v3
	v_rcp_iflag_f32_e32 v5, v5
	v_add_u32_e32 v6, s9, v2
	v_mul_f32_e32 v5, 0x4f7ffffe, v5
	v_cvt_u32_f32_e32 v5, v5
	v_mul_lo_u32 v2, v4, v5
	v_mul_hi_u32 v2, v5, v2
	v_add_u32_e32 v2, v5, v2
	v_mul_hi_u32 v2, v6, v2
	v_mul_lo_u32 v4, v2, v3
	v_sub_u32_e32 v4, v6, v4
	v_add_u32_e32 v5, 1, v2
	v_cmp_ge_u32_e32 vcc, v4, v3
	s_nop 1
	v_cndmask_b32_e32 v2, v2, v5, vcc
	v_sub_u32_e32 v5, v4, v3
	v_cndmask_b32_e32 v4, v4, v5, vcc
	v_add_u32_e32 v5, 1, v2
	v_cmp_ge_u32_e32 vcc, v4, v3
	v_add_u32_e32 v4, 1, v6
	s_nop 0
	v_cndmask_b32_e32 v2, v2, v5, vcc
	v_mul_lo_u32 v5, v3, v2
	v_add_u32_e32 v3, v5, v3
	v_cmp_ne_u32_e32 vcc, v4, v3
	v_mov_b32_e32 v19, v2
	s_and_saveexec_b64 s[10:11], vcc
	s_xor_b64 s[10:11], exec, s[10:11]
	s_cbranch_execz .LBB0_561
	s_waitcnt lgkmcnt(0)
	v_mov_b32_e32 v1, 0x2000
	global_load_dword v1, v1, s[2:3] offset:1024 sc1
	s_add_u32 s16, s2, 0x2400
	s_addc_u32 s17, s3, 0
	s_waitcnt vmcnt(0)
	v_cmp_eq_u32_e32 vcc, v1, v2
	s_and_saveexec_b64 s[12:13], vcc
	s_cbranch_execz .LBB0_560
	s_add_u32 s14, s26, 0x4200
	s_addc_u32 s15, s27, 0
	s_mov_b32 s9, 1
	s_mov_b64 s[18:19], 0
	v_mov_b32_e32 v1, 0
	s_branch .LBB0_551

; __device__ __forceinline__ unsigned xb_ld(unsigned* p)              { return __hip_atomic_load(p, __ATOMIC_RELAXED, __HIP_MEMORY_SCOPE_AGENT); }
; __device__ __forceinline__ unsigned xb_add(unsigned* p, unsigned v) { return __hip_atomic_fetch_add(p, v, __ATOMIC_RELAXED, __HIP_MEMORY_SCOPE_AGENT); }
; #define XB_SPIN(cond, bar) do { unsigned _sp = 0; while (cond) { __builtin_amdgcn_s_sleep(1); \
;     if ((++_sp & 255u) == 0u) { if (xb_ld(&(bar)[XB_TMO])) break; if (_sp > XB_SPIN_CAP) { atomicAdd(&(bar)[XB_TMO], 1u); break; } } } } while (0)
; __device__ __forceinline__ void xcd_barrier(const XcdBarrier& b) {
;     ...
;             const unsigned og = xb_add(&bar[XB_TOP], 1u);
;             const unsigned tg = og / nx;
;             if (og + 1u == (tg + 1u) * nx) xb_add(&bar[XB_TOPGEN], 1u);
;             else XB_SPIN(xb_ld(&bar[XB_TOPGEN]) == tg, bar);
.LBB0_564:
	s_or_b64 exec, exec, s[12:13]
	v_cvt_f32_u32_e32 v4, v1
	s_waitcnt vmcnt(0)
	v_readfirstlane_b32 s9, v3
	s_add_u32 s12, s26, 0x7500
	s_addc_u32 s13, s27, 0
	v_rcp_iflag_f32_e32 v4, v4
	v_add_u32_e32 v2, s9, v2
	v_add_u32_e32 v5, 1, v2
	s_mov_b64 s[14:15], -1
	v_mul_f32_e32 v3, 0x4f7ffffe, v4
	v_cvt_u32_f32_e32 v3, v3
	v_sub_u32_e32 v4, 0, v1
	v_mul_lo_u32 v4, v4, v3
	v_mul_hi_u32 v4, v3, v4
	v_add_u32_e32 v3, v3, v4
	v_mul_hi_u32 v3, v2, v3
	v_mul_lo_u32 v4, v3, v1
	v_sub_u32_e32 v2, v2, v4
	v_add_u32_e32 v6, 1, v3
	v_cmp_ge_u32_e32 vcc, v2, v1
	v_sub_u32_e32 v4, v2, v1
	s_nop 0
	v_cndmask_b32_e32 v3, v3, v6, vcc
	v_cndmask_b32_e32 v2, v2, v4, vcc
	v_add_u32_e32 v4, 1, v3
	v_cmp_ge_u32_e32 vcc, v2, v1
	s_nop 1
	v_cndmask_b32_e32 v4, v3, v4, vcc
	v_mul_lo_u32 v2, v1, v4
	v_add_u32_e32 v1, v2, v1
	v_cmp_ne_u32_e32 vcc, v5, v1
	v_mov_b64_e32 v[2:3], s[12:13]
	s_and_saveexec_b64 s[10:11], vcc
	s_cbranch_execz .LBB0_576
	v_mov_b32_e32 v1, 0
	v_mov_b32_e32 v20, 0x2000
	global_load_dword v2, v20, s[2:3] offset:1024 sc1
	s_mov_b64 s[18:19], 0
	s_waitcnt vmcnt(0)
	v_cmp_eq_u32_e32 vcc, v2, v19
	s_and_saveexec_b64 s[16:17], vcc
	s_cbranch_execz .LBB0_575
	s_add_u32 s14, s26, 0x4200
	s_addc_u32 s15, s27, 0
	s_mov_b32 s9, 1
	s_branch .LBB0_568

; __device__ __forceinline__ unsigned xb_ld(unsigned* p)              { return __hip_atomic_load(p, __ATOMIC_RELAXED, __HIP_MEMORY_SCOPE_AGENT); }
; __device__ __forceinline__ unsigned xb_add(unsigned* p, unsigned v) { return __hip_atomic_fetch_add(p, v, __ATOMIC_RELAXED, __HIP_MEMORY_SCOPE_AGENT); }
; #define XB_SPIN(cond, bar) do { unsigned _sp = 0; while (cond) { __builtin_amdgcn_s_sleep(1); \
;     if ((++_sp & 255u) == 0u) { if (xb_ld(&(bar)[XB_TMO])) break; if (_sp > XB_SPIN_CAP) { atomicAdd(&(bar)[XB_TMO], 1u); break; } } } } while (0)
; __device__ __forceinline__ void xcd_barrier(const XcdBarrier& b) {
;     ...
;             if (og + 1u == (tg + 1u) * nx) xb_add(&bar[XB_TOPGEN], 1u);
;             else XB_SPIN(xb_ld(&bar[XB_TOPGEN]) == tg, bar);
.LBB0_570:
	global_load_dword v2, v20, s[2:3] offset:1024 sc1
	s_add_i32 s9, s9, 1
	s_mov_b64 s[22:23], -1
	s_waitcnt vmcnt(0)
	v_cmp_ne_u32_e32 vcc, v2, v19
	s_orn2_b64 s[42:43], vcc, exec
	s_branch .LBB0_567

; __device__ __forceinline__ unsigned xb_ld(unsigned* p)              { return __hip_atomic_load(p, __ATOMIC_RELAXED, __HIP_MEMORY_SCOPE_AGENT); }
; __device__ __forceinline__ unsigned xb_add(unsigned* p, unsigned v) { return __hip_atomic_fetch_add(p, v, __ATOMIC_RELAXED, __HIP_MEMORY_SCOPE_AGENT); }
; #define XB_SPIN(cond, bar) do { unsigned _sp = 0; while (cond) { __builtin_amdgcn_s_sleep(1); \
;     if ((++_sp & 255u) == 0u) { if (xb_ld(&(bar)[XB_TMO])) break; if (_sp > XB_SPIN_CAP) { atomicAdd(&(bar)[XB_TMO], 1u); break; } } } } while (0)
; __device__ __forceinline__ void xcd_barrier(const XcdBarrier& b) {
;     ...
;         const unsigned old = xb_add(&bar[XB_XSUB(b.x)], 1u);
;         const unsigned gen = old / nloc;
;         if (old + 1u == (gen + 1u) * nloc) {
;             __builtin_amdgcn_fence(__ATOMIC_RELEASE, "agent");
;             asm volatile("s_waitcnt vmcnt(0)" ::: "memory");
;             const unsigned og = xb_add(&bar[XB_TOP], 1u);
;             const unsigned tg = og / nx;
;             if (og + 1u == (tg + 1u) * nx) xb_add(&bar[XB_TOPGEN], 1u);
;             else XB_SPIN(xb_ld(&bar[XB_TOPGEN]) == tg, bar);
;             __builtin_amdgcn_fence(__ATOMIC_ACQUIRE, "agent");
;             xb_add(&bar[XB_XGEN(b.x)], 1u);
;             asm volatile("s_waitcnt vmcnt(0)" ::: "memory");
;         } else {
;             XB_SPIN(xb_ld(&bar[XB_XGEN(b.x)]) == gen, bar);
.LBB0_1409:
	s_or_b64 exec, exec, s[10:11]
	v_cvt_f32_u32_e32 v5, v3
	s_waitcnt vmcnt(0)
	v_readfirstlane_b32 s8, v4
	v_sub_u32_e32 v4, 0, v3
	v_rcp_iflag_f32_e32 v5, v5
	v_add_u32_e32 v6, s8, v2
	v_mul_f32_e32 v5, 0x4f7ffffe, v5
	v_cvt_u32_f32_e32 v5, v5
	v_mul_lo_u32 v2, v4, v5
	v_mul_hi_u32 v2, v5, v2
	v_add_u32_e32 v2, v5, v2
	v_mul_hi_u32 v2, v6, v2
	v_mul_lo_u32 v4, v2, v3
	v_sub_u32_e32 v4, v6, v4
	v_add_u32_e32 v5, 1, v2
	v_cmp_ge_u32_e32 vcc, v4, v3
	s_nop 1
	v_cndmask_b32_e32 v2, v2, v5, vcc
	v_sub_u32_e32 v5, v4, v3
	v_cndmask_b32_e32 v4, v4, v5, vcc
	v_add_u32_e32 v5, 1, v2
	v_cmp_ge_u32_e32 vcc, v4, v3
	v_add_u32_e32 v4, 1, v6
	s_nop 0
	v_cndmask_b32_e32 v2, v2, v5, vcc
	v_mul_lo_u32 v5, v3, v2
	v_add_u32_e32 v3, v5, v3
	v_cmp_ne_u32_e32 vcc, v4, v3
	v_mov_b32_e32 v19, v2
	s_and_saveexec_b64 s[8:9], vcc
	s_xor_b64 s[8:9], exec, s[8:9]
	s_cbranch_execz .LBB0_1423
	s_waitcnt lgkmcnt(0)
	v_mov_b32_e32 v1, 0x2000
	global_load_dword v1, v1, s[2:3] offset:1024 sc1
	s_add_u32 s14, s2, 0x2400
	s_addc_u32 s15, s3, 0
	s_waitcnt vmcnt(0)
	v_cmp_eq_u32_e32 vcc, v1, v2
	s_and_saveexec_b64 s[10:11], vcc
	s_cbranch_execz .LBB0_1422
	s_add_u32 s12, s26, 0x4200
	s_addc_u32 s13, s27, 0
	s_mov_b32 s42, 1
	s_mov_b64 s[16:17], 0
	v_mov_b32_e32 v1, 0
	s_branch .LBB0_1413

; __device__ __forceinline__ unsigned xb_ld(unsigned* p)              { return __hip_atomic_load(p, __ATOMIC_RELAXED, __HIP_MEMORY_SCOPE_AGENT); }
; __device__ __forceinline__ unsigned xb_add(unsigned* p, unsigned v) { return __hip_atomic_fetch_add(p, v, __ATOMIC_RELAXED, __HIP_MEMORY_SCOPE_AGENT); }
; #define XB_SPIN(cond, bar) do { unsigned _sp = 0; while (cond) { __builtin_amdgcn_s_sleep(1); \
;     if ((++_sp & 255u) == 0u) { if (xb_ld(&(bar)[XB_TMO])) break; if (_sp > XB_SPIN_CAP) { atomicAdd(&(bar)[XB_TMO], 1u); break; } } } } while (0)
; __device__ __forceinline__ void xcd_barrier(const XcdBarrier& b) {
;     ...
;             const unsigned og = xb_add(&bar[XB_TOP], 1u);
;             const unsigned tg = og / nx;
;             if (og + 1u == (tg + 1u) * nx) xb_add(&bar[XB_TOPGEN], 1u);
;             else XB_SPIN(xb_ld(&bar[XB_TOPGEN]) == tg, bar);
.LBB0_1426:
	s_or_b64 exec, exec, s[10:11]
	v_cvt_f32_u32_e32 v4, v1
	s_waitcnt vmcnt(0)
	v_readfirstlane_b32 s8, v3
	s_add_u32 s10, s26, 0x7500
	s_addc_u32 s11, s27, 0
	v_rcp_iflag_f32_e32 v4, v4
	v_add_u32_e32 v2, s8, v2
	v_add_u32_e32 v5, 1, v2
	s_mov_b64 s[12:13], -1
	v_mul_f32_e32 v3, 0x4f7ffffe, v4
	v_cvt_u32_f32_e32 v3, v3
	v_sub_u32_e32 v4, 0, v1
	v_mul_lo_u32 v4, v4, v3
	v_mul_hi_u32 v4, v3, v4
	v_add_u32_e32 v3, v3, v4
	v_mul_hi_u32 v3, v2, v3
	v_mul_lo_u32 v4, v3, v1
	v_sub_u32_e32 v2, v2, v4
	v_add_u32_e32 v6, 1, v3
	v_cmp_ge_u32_e32 vcc, v2, v1
	v_sub_u32_e32 v4, v2, v1
	s_nop 0
	v_cndmask_b32_e32 v3, v3, v6, vcc
	v_cndmask_b32_e32 v2, v2, v4, vcc
	v_add_u32_e32 v4, 1, v3
	v_cmp_ge_u32_e32 vcc, v2, v1
	s_nop 1
	v_cndmask_b32_e32 v4, v3, v4, vcc
	v_mul_lo_u32 v2, v1, v4
	v_add_u32_e32 v1, v2, v1
	v_cmp_ne_u32_e32 vcc, v5, v1
	v_mov_b64_e32 v[2:3], s[10:11]
	s_and_saveexec_b64 s[8:9], vcc
	s_cbranch_execz .LBB0_1438
	v_mov_b32_e32 v1, 0
	v_mov_b32_e32 v20, 0x2000
	global_load_dword v2, v20, s[2:3] offset:1024 sc1
	s_mov_b64 s[16:17], 0
	s_waitcnt vmcnt(0)
	v_cmp_eq_u32_e32 vcc, v2, v19
	s_and_saveexec_b64 s[14:15], vcc
	s_cbranch_execz .LBB0_1437
	s_add_u32 s12, s26, 0x4200
	s_addc_u32 s13, s27, 0
	s_mov_b32 s42, 1
	s_branch .LBB0_1430

; __device__ __forceinline__ unsigned xb_ld(unsigned* p)              { return __hip_atomic_load(p, __ATOMIC_RELAXED, __HIP_MEMORY_SCOPE_AGENT); }
; __device__ __forceinline__ unsigned xb_add(unsigned* p, unsigned v) { return __hip_atomic_fetch_add(p, v, __ATOMIC_RELAXED, __HIP_MEMORY_SCOPE_AGENT); }
; #define XB_SPIN(cond, bar) do { unsigned _sp = 0; while (cond) { __builtin_amdgcn_s_sleep(1); \
;     if ((++_sp & 255u) == 0u) { if (xb_ld(&(bar)[XB_TMO])) break; if (_sp > XB_SPIN_CAP) { atomicAdd(&(bar)[XB_TMO], 1u); break; } } } } while (0)
; __device__ __forceinline__ void xcd_barrier(const XcdBarrier& b) {
;     ...
;             if (og + 1u == (tg + 1u) * nx) xb_add(&bar[XB_TOPGEN], 1u);
;             else XB_SPIN(xb_ld(&bar[XB_TOPGEN]) == tg, bar);
.LBB0_1432:
	global_load_dword v2, v20, s[2:3] offset:1024 sc1
	s_add_i32 s42, s42, 1
	s_mov_b64 s[20:21], -1
	s_waitcnt vmcnt(0)
	v_cmp_ne_u32_e32 vcc, v2, v19
	s_orn2_b64 s[40:41], vcc, exec
	s_branch .LBB0_1429

; __device__ __forceinline__ unsigned xb_ld(unsigned* p)              { return __hip_atomic_load(p, __ATOMIC_RELAXED, __HIP_MEMORY_SCOPE_AGENT); }
; __device__ __forceinline__ unsigned xb_add(unsigned* p, unsigned v) { return __hip_atomic_fetch_add(p, v, __ATOMIC_RELAXED, __HIP_MEMORY_SCOPE_AGENT); }
; #define XB_SPIN(cond, bar) do { unsigned _sp = 0; while (cond) { __builtin_amdgcn_s_sleep(1); \
;     if ((++_sp & 255u) == 0u) { if (xb_ld(&(bar)[XB_TMO])) break; if (_sp > XB_SPIN_CAP) { atomicAdd(&(bar)[XB_TMO], 1u); break; } } } } while (0)
; __device__ __forceinline__ void xcd_barrier(const XcdBarrier& b) {
;     ...
;             if (og + 1u == (tg + 1u) * nx) xb_add(&bar[XB_TOPGEN], 1u);
;             else XB_SPIN(xb_ld(&bar[XB_TOPGEN]) == tg, bar);
;             __builtin_amdgcn_fence(__ATOMIC_ACQUIRE, "agent");
;             xb_add(&bar[XB_XGEN(b.x)], 1u);
;             asm volatile("s_waitcnt vmcnt(0)" ::: "memory");
.LBB0_1438:
	s_or_b64 exec, exec, s[8:9]
	s_and_saveexec_b64 s[8:9], s[12:13]
	s_cbranch_execz .LBB0_1440
	v_mov_b32_e32 v1, 1
	global_atomic_add v[2:3], v1, off
	v_mov_b32_e32 v21, 0x2000
	v_mov_b32_e32 v22, 1
	s_mov_b64 s[10:11], s[28:29]
	s_movk_i32 vcc_lo, 16
.Lbh13_loop:
	global_atomic_add v21, v22, s[10:11] offset:1024
	s_add_u32 s10, s10, 0x100
	s_addc_u32 s11, s11, 0
	s_sub_i32 vcc_lo, vcc_lo, 1
	s_cmp_lg_u32 vcc_lo, 0
	s_cbranch_scc1 .Lbh13_loop
.LBB0_1440:
	s_or_b64 exec, exec, s[8:9]
	s_mov_b64 s[8:9], exec
	v_mbcnt_lo_u32_b32 v1, s8, 0
	v_mbcnt_hi_u32_b32 v1, s9, v1
	v_cmp_eq_u32_e32 vcc, 0, v1
	s_waitcnt vmcnt(0)
	buffer_inv sc1
	s_and_saveexec_b64 s[10:11], vcc
	s_cbranch_execz .LBB0_1442
	s_bcnt1_i32_b64 s8, s[8:9]
	v_mov_b32_e32 v1, 0x2000
	v_mov_b32_e32 v2, s8
	s_nop 0

; __device__ __forceinline__ unsigned xb_ld(unsigned* p)              { return __hip_atomic_load(p, __ATOMIC_RELAXED, __HIP_MEMORY_SCOPE_AGENT); }
; __device__ __forceinline__ unsigned xb_add(unsigned* p, unsigned v) { return __hip_atomic_fetch_add(p, v, __ATOMIC_RELAXED, __HIP_MEMORY_SCOPE_AGENT); }
; #define XB_SPIN(cond, bar) do { unsigned _sp = 0; while (cond) { __builtin_amdgcn_s_sleep(1); \
;     if ((++_sp & 255u) == 0u) { if (xb_ld(&(bar)[XB_TMO])) break; if (_sp > XB_SPIN_CAP) { atomicAdd(&(bar)[XB_TMO], 1u); break; } } } } while (0)
; __device__ __forceinline__ void xcd_barrier(const XcdBarrier& b) {
;     ...
;         const unsigned old = xb_add(&bar[XB_XSUB(b.x)], 1u);
;         const unsigned gen = old / nloc;
;         if (old + 1u == (gen + 1u) * nloc) {
;             __builtin_amdgcn_fence(__ATOMIC_RELEASE, "agent");
;             asm volatile("s_waitcnt vmcnt(0)" ::: "memory");
;             const unsigned og = xb_add(&bar[XB_TOP], 1u);
;             const unsigned tg = og / nx;
;             if (og + 1u == (tg + 1u) * nx) xb_add(&bar[XB_TOPGEN], 1u);
;             else XB_SPIN(xb_ld(&bar[XB_TOPGEN]) == tg, bar);
;             __builtin_amdgcn_fence(__ATOMIC_ACQUIRE, "agent");
;             xb_add(&bar[XB_XGEN(b.x)], 1u);
;             asm volatile("s_waitcnt vmcnt(0)" ::: "memory");
;         } else {
;             XB_SPIN(xb_ld(&bar[XB_XGEN(b.x)]) == gen, bar);
.LBB0_1551:
	s_or_b64 exec, exec, s[10:11]
	v_cvt_f32_u32_e32 v5, v3
	s_waitcnt vmcnt(0)
	v_readfirstlane_b32 s8, v4
	v_sub_u32_e32 v4, 0, v3
	v_rcp_iflag_f32_e32 v5, v5
	v_add_u32_e32 v6, s8, v2
	v_mul_f32_e32 v5, 0x4f7ffffe, v5
	v_cvt_u32_f32_e32 v5, v5
	v_mul_lo_u32 v2, v4, v5
	v_mul_hi_u32 v2, v5, v2
	v_add_u32_e32 v2, v5, v2
	v_mul_hi_u32 v2, v6, v2
	v_mul_lo_u32 v4, v2, v3
	v_sub_u32_e32 v4, v6, v4
	v_add_u32_e32 v5, 1, v2
	v_cmp_ge_u32_e32 vcc, v4, v3
	s_nop 1
	v_cndmask_b32_e32 v2, v2, v5, vcc
	v_sub_u32_e32 v5, v4, v3
	v_cndmask_b32_e32 v4, v4, v5, vcc
	v_add_u32_e32 v5, 1, v2
	v_cmp_ge_u32_e32 vcc, v4, v3
	v_add_u32_e32 v4, 1, v6
	s_nop 0
	v_cndmask_b32_e32 v2, v2, v5, vcc
	v_mul_lo_u32 v5, v3, v2
	v_add_u32_e32 v3, v5, v3
	v_cmp_ne_u32_e32 vcc, v4, v3
	v_mov_b32_e32 v19, v2
	s_and_saveexec_b64 s[8:9], vcc
	s_xor_b64 s[8:9], exec, s[8:9]
	s_cbranch_execz .LBB0_1565
	s_waitcnt lgkmcnt(0)
	v_mov_b32_e32 v1, 0x2000
	global_load_dword v1, v1, s[4:5] offset:1024 sc1
	s_add_u32 s14, s4, 0x2400
	s_addc_u32 s15, s5, 0
	s_waitcnt vmcnt(0)
	v_cmp_eq_u32_e32 vcc, v1, v2
	s_and_saveexec_b64 s[10:11], vcc
	s_cbranch_execz .LBB0_1564
	s_add_u32 s12, s26, 0x4200
	s_addc_u32 s13, s27, 0
	s_mov_b32 s42, 1
	s_mov_b64 s[16:17], 0
	v_mov_b32_e32 v1, 0
	s_branch .LBB0_1555

; __device__ __forceinline__ unsigned xb_ld(unsigned* p)              { return __hip_atomic_load(p, __ATOMIC_RELAXED, __HIP_MEMORY_SCOPE_AGENT); }
; __device__ __forceinline__ unsigned xb_add(unsigned* p, unsigned v) { return __hip_atomic_fetch_add(p, v, __ATOMIC_RELAXED, __HIP_MEMORY_SCOPE_AGENT); }
; #define XB_SPIN(cond, bar) do { unsigned _sp = 0; while (cond) { __builtin_amdgcn_s_sleep(1); \
;     if ((++_sp & 255u) == 0u) { if (xb_ld(&(bar)[XB_TMO])) break; if (_sp > XB_SPIN_CAP) { atomicAdd(&(bar)[XB_TMO], 1u); break; } } } } while (0)
; __device__ __forceinline__ void xcd_barrier(const XcdBarrier& b) {
;     ...
;             const unsigned og = xb_add(&bar[XB_TOP], 1u);
;             const unsigned tg = og / nx;
;             if (og + 1u == (tg + 1u) * nx) xb_add(&bar[XB_TOPGEN], 1u);
;             else XB_SPIN(xb_ld(&bar[XB_TOPGEN]) == tg, bar);
.LBB0_1568:
	s_or_b64 exec, exec, s[10:11]
	v_cvt_f32_u32_e32 v4, v1
	s_waitcnt vmcnt(0)
	v_readfirstlane_b32 s8, v3
	s_add_u32 s10, s26, 0x7500
	s_addc_u32 s11, s27, 0
	v_rcp_iflag_f32_e32 v4, v4
	v_add_u32_e32 v2, s8, v2
	v_add_u32_e32 v5, 1, v2
	s_mov_b64 s[12:13], -1
	v_mul_f32_e32 v3, 0x4f7ffffe, v4
	v_cvt_u32_f32_e32 v3, v3
	v_sub_u32_e32 v4, 0, v1
	v_mul_lo_u32 v4, v4, v3
	v_mul_hi_u32 v4, v3, v4
	v_add_u32_e32 v3, v3, v4
	v_mul_hi_u32 v3, v2, v3
	v_mul_lo_u32 v4, v3, v1
	v_sub_u32_e32 v2, v2, v4
	v_add_u32_e32 v6, 1, v3
	v_cmp_ge_u32_e32 vcc, v2, v1
	v_sub_u32_e32 v4, v2, v1
	s_nop 0
	v_cndmask_b32_e32 v3, v3, v6, vcc
	v_cndmask_b32_e32 v2, v2, v4, vcc
	v_add_u32_e32 v4, 1, v3
	v_cmp_ge_u32_e32 vcc, v2, v1
	s_nop 1
	v_cndmask_b32_e32 v4, v3, v4, vcc
	v_mul_lo_u32 v2, v1, v4
	v_add_u32_e32 v1, v2, v1
	v_cmp_ne_u32_e32 vcc, v5, v1
	v_mov_b64_e32 v[2:3], s[10:11]
	s_and_saveexec_b64 s[8:9], vcc
	s_cbranch_execz .LBB0_1580
	v_mov_b32_e32 v1, 0
	v_mov_b32_e32 v20, 0x2000
	global_load_dword v2, v20, s[4:5] offset:1024 sc1
	s_mov_b64 s[16:17], 0
	s_waitcnt vmcnt(0)
	v_cmp_eq_u32_e32 vcc, v2, v19
	s_and_saveexec_b64 s[14:15], vcc
	s_cbranch_execz .LBB0_1579
	s_add_u32 s12, s26, 0x4200
	s_addc_u32 s13, s27, 0
	s_mov_b32 s42, 1
	s_branch .LBB0_1572

; __device__ __forceinline__ unsigned xb_ld(unsigned* p)              { return __hip_atomic_load(p, __ATOMIC_RELAXED, __HIP_MEMORY_SCOPE_AGENT); }
; __device__ __forceinline__ unsigned xb_add(unsigned* p, unsigned v) { return __hip_atomic_fetch_add(p, v, __ATOMIC_RELAXED, __HIP_MEMORY_SCOPE_AGENT); }
; #define XB_SPIN(cond, bar) do { unsigned _sp = 0; while (cond) { __builtin_amdgcn_s_sleep(1); \
;     if ((++_sp & 255u) == 0u) { if (xb_ld(&(bar)[XB_TMO])) break; if (_sp > XB_SPIN_CAP) { atomicAdd(&(bar)[XB_TMO], 1u); break; } } } } while (0)
; __device__ __forceinline__ void xcd_barrier(const XcdBarrier& b) {
;     ...
;             if (og + 1u == (tg + 1u) * nx) xb_add(&bar[XB_TOPGEN], 1u);
;             else XB_SPIN(xb_ld(&bar[XB_TOPGEN]) == tg, bar);
.LBB0_1574:
	global_load_dword v2, v20, s[4:5] offset:1024 sc1
	s_add_i32 s42, s42, 1
	s_mov_b64 s[20:21], -1
	s_waitcnt vmcnt(0)
	v_cmp_ne_u32_e32 vcc, v2, v19
	s_orn2_b64 s[40:41], vcc, exec
	s_branch .LBB0_1571
